# conversion queue: each wave claims its next chunk ahead of time (atomic issued at the previous claim, result read at the next), chunk 4
# baseline (speedup 1.0000x reference)
; #define RI_NEXT(D_) do { if (q.cnt == 8) { int b_ = 0; if (F.lane == 0) b_ = (int)__hip_atomic_fetch_add(qctr, 8u, __ATOMIC_RELAXED, __HIP_MEMORY_SCOPE_AGENT); q.base = __builtin_amdgcn_readfirstlane(b_); q.cnt = 0; } \
;         D_ = decode_item(KA, F.ws, kind, q.base + q.cnt); ++q.cnt; } while (0)
; DI void run_items1(Frame& F, int kind, int quota, QState& q) {
;     ...
;     if (quota == 0) return;
;     TItem d; RI_NEXT(d); if (!d.valid) return;
; DI void phase_attn(Frame& F, int l) {
;     ...
;     QState cq; cq.base = 0; cq.cnt = 8;
;     constexpr int SLOT_ITEMS = 3;
;     if (F.bid & 1) { __syncthreads(); run_items1(F, 1 + l, SLOT_ITEMS, cq); }
.LBB0_398:
	v_readlane_b32 s8, v255, 14
	v_readlane_b32 s4, v253, 8
	s_lshl_b32 s58, s8, 6
	v_readlane_b32 s6, v253, 10
	v_readlane_b32 s7, v253, 11
	s_lshl_b64 s[0:1], s[58:59], 2
	s_mov_b64 s[2:3], s[6:7]
	s_add_u32 s0, s2, s0
	s_addc_u32 s1, s3, s1
	v_readlane_b32 s9, v255, 15
	s_add_u32 s12, s0, 0x8100
	s_addc_u32 s13, s1, 0
	s_lshl_b64 s[0:1], s[8:9], 25
	v_writelane_b32 v255, s0, 16
	s_lshl_b64 s[62:63], s[8:9], 5
	s_lshl_b32 s2, s8, 20
	v_writelane_b32 v255, s1, 17
	s_mov_b32 s3, s59
	v_readlane_b32 s0, v253, 33
	v_writelane_b32 v255, s2, 18
	s_add_u32 s76, s0, s2
	v_readlane_b32 s0, v253, 34
	v_writelane_b32 v255, s3, 19
	s_addc_u32 s77, s0, 0
	s_lshl_b64 s[20:21], s[8:9], 21
	s_lshl_b64 s[0:1], s[8:9], 20
	v_readlane_b32 s2, v253, 35
	s_add_u32 s22, s2, s0
	v_readlane_b32 s2, v253, 36
	s_addc_u32 s23, s2, s1
	v_readlane_b32 s2, v253, 37
	s_add_u32 s24, s2, s0
	v_readlane_b32 s0, v253, 38
	s_addc_u32 s25, s0, s1
	s_lshl_b64 s[26:27], s[8:9], 24
	v_readlane_b32 s0, v253, 39
	s_add_u32 s14, s0, s44
	v_readlane_b32 s0, v253, 40
	s_addc_u32 s15, s0, s45
	s_mov_b32 s0, -1
	s_mov_b32 s95, 0
	v_mbcnt_lo_u32_b32 v0, s0, 0
	v_mbcnt_hi_u32_b32 v186, s0, v0
	v_readlane_b32 s0, v253, 29
	s_mov_b32 s51, s0
	s_mov_b64 s[0:1], exec
	s_mov_b64 exec, 1
	v_mov_b32_e32 v206, 4
	global_atomic_add v206, v1, v206, s[12:13] sc0
	s_mov_b64 exec, s[0:1]
	s_mov_b64 s[30:31], s[70:71]
	s_bitcmp0_b32 s51, 0
	s_mov_b32 s63, 4
	v_readlane_b32 s5, v253, 9
	v_readlane_b32 s1, v253, 30
	s_cbranch_scc1 .LBB0_472
	s_mov_b64 s[6:7], s[70:71]
	v_mov_b32_e32 v0, 0
	v_cmp_eq_u32_e64 s[4:5], 0, v186
	s_waitcnt vmcnt(63) expcnt(7) lgkmcnt(15)
	s_barrier
	s_waitcnt vmcnt(0)
	v_readfirstlane_b32 s95, v206
	s_mov_b64 s[2:3], exec
	s_mov_b64 exec, 1
	v_mov_b32_e32 v206, 4
	global_atomic_add v206, v1, v206, s[12:13] sc0
	s_mov_b64 exec, s[2:3]
	s_cmpk_lt_i32 s95, 0x6000
	s_cselect_b64 s[2:3], -1, 0
	s_and_b64 s[0:1], s[2:3], exec
	s_cselect_b32 s36, s95, 0
	s_add_i32 s0, s36, 0x680
	s_cmpk_gt_i32 s36, 0xfd7f
	s_mov_b64 s[18:19], -1
	s_cbranch_scc0 .LBB0_424
	s_mov_b64 s[34:35], -1
	s_cmpk_gt_u32 s0, 0x47f
	s_mov_b64 s[8:9], -1
	s_cbranch_scc0 .LBB0_421
	s_cmpk_gt_u32 s0, 0x4ff
	s_cbranch_scc0 .LBB0_418
	s_cmpk_gt_u32 s0, 0x57f
	s_cbranch_scc0 .LBB0_415
	s_cmp_lt_u32 s36, 0xfffff980
	s_cbranch_scc0 .LBB0_412
	s_mov_b64 s[28:29], -1
	s_cmpk_gt_u32 s0, 0x467f
	s_cbranch_scc0 .LBB0_410
	s_add_i32 s1, s36, 0xffffc000
	s_lshr_b32 s58, s1, 8
	s_load_dwordx2 s[8:9], s[6:7], 0xd0
	s_and_b32 s1, s36, 0xff
	s_lshl_b64 s[10:11], s[58:59], 20
	v_readlane_b32 s16, v255, 16
	v_readlane_b32 s17, v255, 17
	s_add_u32 s10, s10, s16
	s_addc_u32 s11, s11, s17
	s_lshl_b64 s[16:17], s[10:11], 2
	s_waitcnt lgkmcnt(0)
	s_add_u32 s16, s8, s16
	s_addc_u32 s17, s9, s17
	v_readlane_b32 s8, v253, 45
	s_add_u32 s10, s8, s10
	v_readlane_b32 s8, v253, 46
	s_addc_u32 s11, s8, s11
	s_mov_b64 s[8:9], 0

; #define LDS_WAIT() asm volatile("s_waitcnt lgkmcnt(0)" ::: "memory")
; #define RI_NEXT(D_) do { if (q.cnt == 8) { int b_ = 0; if (F.lane == 0) b_ = (int)__hip_atomic_fetch_add(qctr, 8u, __ATOMIC_RELAXED, __HIP_MEMORY_SCOPE_AGENT); q.base = __builtin_amdgcn_readfirstlane(b_); q.cnt = 0; } \
;         D_ = decode_item(KA, F.ws, kind, q.base + q.cnt); ++q.cnt; } while (0)
; DI void item_scatter(const f32x4 (&v)[16], LAS float* scr, int lane) {
;     ...
;     for (int i = 0; i < 16; ++i) { const int k = 4 * i + r4;
; #pragma unroll
;         for (int j = 0; j < 4; ++j) scr[(4 * c4 + j) * 64 + (k ^ (4 * (c4 ^ j)))] = v[i][j]; }
;     LDS_WAIT(); asm volatile("" ::: "memory");
; DI void run_items1(Frame& F, int kind, int quota, QState& q) {
;     ...
;         item_scatter(v, scr, F.lane);
;         TItem dn; dn.valid = false;
;         if (quota < 0 || n < quota) { RI_NEXT(dn); if (dn.valid) item_load(dn, v, F.lane); }
.LBB0_430:
	s_waitcnt vmcnt(0)
	ds_write_b32 v93, v2
	ds_write_b32 v94, v3 offset:256
	ds_write_b32 v95, v4 offset:512
	ds_write_b32 v96, v5 offset:768
	ds_write_b32 v97, v6
	ds_write_b32 v98, v7 offset:256
	ds_write_b32 v99, v8 offset:512
	ds_write_b32 v100, v9 offset:768
	ds_write_b32 v101, v10
	ds_write_b32 v102, v11 offset:256
	ds_write_b32 v103, v12 offset:512
	ds_write_b32 v104, v13 offset:768
	ds_write_b32 v105, v14
	ds_write_b32 v106, v15 offset:256
	ds_write_b32 v107, v16 offset:512
	ds_write_b32 v108, v17 offset:768
	ds_write_b32 v109, v18
	ds_write_b32 v110, v19 offset:256
	ds_write_b32 v111, v20 offset:512
	ds_write_b32 v112, v21 offset:768
	ds_write_b32 v113, v22
	ds_write_b32 v114, v23 offset:256
	ds_write_b32 v115, v24 offset:512
	ds_write_b32 v116, v25 offset:768
	ds_write_b32 v117, v26
	ds_write_b32 v118, v27 offset:256
	ds_write_b32 v119, v28 offset:512
	ds_write_b32 v120, v29 offset:768
	ds_write_b32 v121, v30
	ds_write_b32 v122, v31 offset:256
	ds_write_b32 v123, v32 offset:512
	ds_write_b32 v124, v33 offset:768
	ds_write_b32 v125, v34
	ds_write_b32 v126, v35 offset:256
	ds_write_b32 v127, v36 offset:512
	ds_write_b32 v128, v37 offset:768
	ds_write_b32 v129, v38
	ds_write_b32 v130, v39 offset:256
	ds_write_b32 v131, v40 offset:512
	ds_write_b32 v132, v41 offset:768
	ds_write_b32 v133, v42
	ds_write_b32 v134, v43 offset:256
	ds_write_b32 v135, v44 offset:512
	ds_write_b32 v136, v45 offset:768
	ds_write_b32 v137, v46
	ds_write_b32 v138, v47 offset:256
	ds_write_b32 v139, v48 offset:512
	ds_write_b32 v140, v49 offset:768
	ds_write_b32 v141, v50
	ds_write_b32 v142, v51 offset:256
	ds_write_b32 v143, v52 offset:512
	ds_write_b32 v144, v53 offset:768
	ds_write_b32 v145, v54
	ds_write_b32 v146, v55 offset:256
	ds_write_b32 v147, v56 offset:512
	ds_write_b32 v148, v57 offset:768
	ds_write_b32 v149, v58
	ds_write_b32 v150, v59 offset:256
	ds_write_b32 v151, v60 offset:512
	ds_write_b32 v152, v61 offset:768
	ds_write_b32 v153, v62
	ds_write_b32 v154, v63 offset:256
	ds_write_b32 v155, v64 offset:512
	ds_write_b32 v156, v65 offset:768
	s_waitcnt lgkmcnt(0)
	s_cmp_gt_u32 s38, 2
	s_mov_b64 s[2:3], 0
	s_cbranch_scc1 .LBB0_465
	s_cmp_lg_u32 s63, 4
	s_cbranch_scc1 .LBB0_437
	s_waitcnt vmcnt(0)
	v_readfirstlane_b32 s95, v206
	s_mov_b64 s[2:3], exec
	s_mov_b64 exec, 1
	v_mov_b32_e32 v206, 4
	global_atomic_add v206, v1, v206, s[12:13] sc0
	s_mov_b64 exec, s[2:3]
	s_mov_b32 s63, 0

; DI unsigned pk4_fp8(float a, float b, float c, float d) { int r = 0; r = __builtin_amdgcn_cvt_pk_fp8_f32(sat8(a), sat8(b), r, false); r = __builtin_amdgcn_cvt_pk_fp8_f32(sat8(c), sat8(d), r, true); return (unsigned)r; }
; DI float half_sum(float v) { const auto rr = __builtin_amdgcn_permlane32_swap(__float_as_uint(v), __float_as_uint(v), false, false); return __uint_as_float(rr[0]) + __uint_as_float(rr[1]); }
; DI void phase_attn(Frame& F, int l) {
;     ...
;         const float ltot = half_sum(l_run); const float inv = AZ8_SCALE / ltot;
; #pragma unroll
;         for (int ds = 0; ds < 2; ++ds)
; #pragma unroll
;             for (int g4 = 0; g4 < 4; g4 += 2) {
;                 const unsigned wa = pk4_fp8(o[ds][4 * g4] * inv, o[ds][4 * g4 + 1] * inv, o[ds][4 * g4 + 2] * inv, o[ds][4 * g4 + 3] * inv), wb = pk4_fp8(o[ds][4 * g4 + 4] * inv, o[ds][4 * g4 + 5] * inv, o[ds][4 * g4 + 6] * inv, o[ds][4 * g4 + 7] * inv);
;                 const auto rr = __builtin_amdgcn_permlane32_swap(wa, wb, false, false);
;                 u32x2 w; w.x = rr[0]; w.y = rr[1];
;                 *(u32x2*)(att + qtok * D + h * HD + 32 * ds + 8 * (g4 + hh)) = w; }
;         if (!((F.bid & 1) && it == 3)) { __syncthreads(); run_items1(F, 1 + l, SLOT_ITEMS, cq); }
.LBB0_568:
	v_mov_b32_e32 v0, v11
	s_nop 1
	v_permlane32_swap_b32_e32 v11, v0
	v_add_f32_e32 v0, v11, v0
	s_mov_b32 s2, 0x41000000
	s_waitcnt vmcnt(1)
	v_div_scale_f32 v2, s[0:1], v0, v0, s2
	v_rcp_f32_e32 v3, v2
	v_readlane_b32 s0, v253, 21
	v_readlane_b32 s1, v253, 22
	s_bitcmp1_b32 s19, 0
	v_fma_f32 v4, -v2, v3, 1.0
	v_fmac_f32_e32 v3, v4, v3
	v_div_scale_f32 v4, vcc, s2, v0, s2
	v_mul_f32_e32 v5, v4, v3
	s_waitcnt vmcnt(0)
	v_fma_f32 v6, -v2, v5, v4
	v_fmac_f32_e32 v5, v6, v3
	v_fma_f32 v2, -v2, v5, v4
	v_div_fmas_f32 v2, v2, v3, v5
	v_div_fixup_f32 v0, v2, v0, s2
	v_mul_f32_e32 v2, v16, v0
	v_mul_f32_e32 v3, v17, v0
	v_med3_f32 v5, v2, s53, v204
	v_med3_f32 v3, v3, s53, v204
	v_mov_b32_e32 v2, v1
	v_cvt_pk_fp8_f32 v2, v5, v3
	v_mul_f32_e32 v4, v18, v0
	v_mul_f32_e32 v3, v19, v0
	v_med3_f32 v4, v4, s53, v204
	v_med3_f32 v3, v3, s53, v204
	v_cvt_pk_fp8_f32 v2, v4, v3 op_sel:[0,0,1]
	v_mul_f32_e32 v3, v20, v0
	v_mul_f32_e32 v4, v21, v0
	v_med3_f32 v6, v3, s53, v204
	v_med3_f32 v4, v4, s53, v204
	v_mov_b32_e32 v3, v1
	v_cvt_pk_fp8_f32 v3, v6, v4
	v_mul_f32_e32 v6, v24, v0
	v_mul_f32_e32 v7, v25, v0
	v_med3_f32 v9, v6, s53, v204
	v_med3_f32 v7, v7, s53, v204
	v_mov_b32_e32 v6, v1
	v_cvt_pk_fp8_f32 v6, v9, v7
	v_mul_f32_e32 v8, v26, v0
	v_mul_f32_e32 v7, v27, v0
	v_med3_f32 v8, v8, s53, v204
	v_med3_f32 v7, v7, s53, v204
	v_cvt_pk_fp8_f32 v6, v8, v7 op_sel:[0,0,1]
	v_mul_f32_e32 v7, v28, v0
	v_mul_f32_e32 v8, v29, v0
	v_med3_f32 v10, v7, s53, v204
	v_med3_f32 v8, v8, s53, v204
	v_mov_b32_e32 v7, v1
	v_cvt_pk_fp8_f32 v7, v10, v8
	v_mul_f32_e32 v5, v22, v0
	v_mul_f32_e32 v4, v23, v0
	v_med3_f32 v5, v5, s53, v204
	v_med3_f32 v4, v4, s53, v204
	v_mul_f32_e32 v9, v30, v0
	v_mul_f32_e32 v8, v31, v0
	v_cvt_pk_fp8_f32 v3, v5, v4 op_sel:[0,0,1]
	v_med3_f32 v9, v9, s53, v204
	v_med3_f32 v8, v8, s53, v204
	v_cvt_pk_fp8_f32 v7, v9, v8 op_sel:[0,0,1]
	v_lshl_add_u64 v[4:5], s[0:1], 0, v[170:171]
	v_lshl_add_u64 v[4:5], v[4:5], 0, s[58:59]
	v_permlane32_swap_b32_e32 v2, v3
	v_lshl_add_u64 v[4:5], v[4:5], 0, v[168:169]
	global_store_dwordx2 v[4:5], v[2:3], off
	v_permlane32_swap_b32_e32 v6, v7
	v_mul_f32_e32 v2, v32, v0
	v_mul_f32_e32 v3, v33, v0
	global_store_dwordx2 v[4:5], v[6:7], off offset:16
	v_med3_f32 v7, v2, s53, v204
	v_med3_f32 v3, v3, s53, v204
	v_mov_b32_e32 v2, v1
	v_cvt_pk_fp8_f32 v2, v7, v3
	v_mul_f32_e32 v6, v34, v0
	v_mul_f32_e32 v3, v35, v0
	v_med3_f32 v6, v6, s53, v204
	v_med3_f32 v3, v3, s53, v204
	v_cvt_pk_fp8_f32 v2, v6, v3 op_sel:[0,0,1]
	v_mul_f32_e32 v3, v36, v0
	v_mul_f32_e32 v6, v37, v0
	v_med3_f32 v8, v3, s53, v204
	v_med3_f32 v6, v6, s53, v204
	v_mov_b32_e32 v3, v1
	v_cvt_pk_fp8_f32 v3, v8, v6
	v_mul_f32_e32 v7, v38, v0
	v_mul_f32_e32 v6, v39, v0
	v_med3_f32 v7, v7, s53, v204
	v_med3_f32 v6, v6, s53, v204
	v_cvt_pk_fp8_f32 v3, v7, v6 op_sel:[0,0,1]
	v_mul_f32_e32 v6, v40, v0
	v_mul_f32_e32 v7, v41, v0
	v_med3_f32 v9, v6, s53, v204
	v_med3_f32 v7, v7, s53, v204
	v_mov_b32_e32 v6, v1
	v_cvt_pk_fp8_f32 v6, v9, v7
	v_mul_f32_e32 v8, v42, v0
	v_mul_f32_e32 v7, v43, v0
	v_med3_f32 v8, v8, s53, v204
	v_med3_f32 v7, v7, s53, v204
	v_cvt_pk_fp8_f32 v6, v8, v7 op_sel:[0,0,1]
	v_mul_f32_e32 v7, v44, v0
	v_mul_f32_e32 v8, v45, v0
	v_med3_f32 v10, v7, s53, v204
	v_med3_f32 v8, v8, s53, v204
	v_mov_b32_e32 v7, v1
	v_cvt_pk_fp8_f32 v7, v10, v8
	v_mul_f32_e32 v9, v46, v0
	v_mul_f32_e32 v0, v47, v0
	v_med3_f32 v8, v9, s53, v204
	v_med3_f32 v0, v0, s53, v204
	v_cvt_pk_fp8_f32 v7, v8, v0 op_sel:[0,0,1]
	s_cselect_b64 s[0:1], -1, 0
	s_cmp_eq_u32 s18, 3
	s_cselect_b64 s[2:3], -1, 0
	s_and_b64 s[0:1], s[2:3], s[0:1]
	v_permlane32_swap_b32_e32 v2, v3
	v_permlane32_swap_b32_e32 v6, v7
	s_and_b64 vcc, exec, s[0:1]
	global_store_dwordx2 v[4:5], v[2:3], off offset:32
	global_store_dwordx2 v[4:5], v[6:7], off offset:48
	s_cbranch_vccnz .LBB0_474
	s_mov_b64 s[6:7], s[70:71]
	s_cmp_lg_u32 s63, 4
	s_barrier
	s_cbranch_scc1 .LBB0_575
	s_waitcnt vmcnt(0)
	v_readfirstlane_b32 s95, v206
	s_mov_b64 s[2:3], exec
	s_mov_b64 exec, 1
	v_mov_b32_e32 v206, 4
	global_atomic_add v206, v1, v206, s[12:13] sc0
	s_mov_b64 exec, s[2:3]
	s_mov_b32 s63, 0

; #define LDS_WAIT() asm volatile("s_waitcnt lgkmcnt(0)" ::: "memory")
; #define RI_NEXT(D_) do { if (q.cnt == 8) { int b_ = 0; if (F.lane == 0) b_ = (int)__hip_atomic_fetch_add(qctr, 8u, __ATOMIC_RELAXED, __HIP_MEMORY_SCOPE_AGENT); q.base = __builtin_amdgcn_readfirstlane(b_); q.cnt = 0; } \
;         D_ = decode_item(KA, F.ws, kind, q.base + q.cnt); ++q.cnt; } while (0)
; DI void item_scatter(const f32x4 (&v)[16], LAS float* scr, int lane) {
;     ...
;     for (int i = 0; i < 16; ++i) { const int k = 4 * i + r4;
; #pragma unroll
;         for (int j = 0; j < 4; ++j) scr[(4 * c4 + j) * 64 + (k ^ (4 * (c4 ^ j)))] = v[i][j]; }
;     LDS_WAIT(); asm volatile("" ::: "memory");
; DI void run_items1(Frame& F, int kind, int quota, QState& q) {
;     ...
;         item_scatter(v, scr, F.lane);
;         TItem dn; dn.valid = false;
;         if (quota < 0 || n < quota) { RI_NEXT(dn); if (dn.valid) item_load(dn, v, F.lane); }
.LBB0_602:
	s_waitcnt vmcnt(15)
	ds_write_b32 v93, v2
	ds_write_b32 v94, v3 offset:256
	ds_write_b32 v95, v4 offset:512
	ds_write_b32 v96, v5 offset:768
	s_waitcnt vmcnt(14)
	ds_write_b32 v97, v6
	ds_write_b32 v98, v7 offset:256
	ds_write_b32 v99, v8 offset:512
	ds_write_b32 v100, v9 offset:768
	s_waitcnt vmcnt(13)
	ds_write_b32 v101, v10
	ds_write_b32 v102, v11 offset:256
	ds_write_b32 v103, v12 offset:512
	ds_write_b32 v104, v13 offset:768
	s_waitcnt vmcnt(12)
	ds_write_b32 v105, v14
	ds_write_b32 v106, v15 offset:256
	ds_write_b32 v107, v16 offset:512
	ds_write_b32 v108, v17 offset:768
	s_waitcnt vmcnt(11)
	ds_write_b32 v109, v18
	ds_write_b32 v110, v19 offset:256
	ds_write_b32 v111, v20 offset:512
	ds_write_b32 v112, v21 offset:768
	s_waitcnt vmcnt(10)
	ds_write_b32 v113, v22
	ds_write_b32 v114, v23 offset:256
	ds_write_b32 v115, v24 offset:512
	ds_write_b32 v116, v25 offset:768
	s_waitcnt vmcnt(9)
	ds_write_b32 v117, v26
	ds_write_b32 v118, v27 offset:256
	ds_write_b32 v119, v28 offset:512
	ds_write_b32 v120, v29 offset:768
	s_waitcnt vmcnt(8)
	ds_write_b32 v121, v30
	ds_write_b32 v122, v31 offset:256
	ds_write_b32 v123, v32 offset:512
	ds_write_b32 v124, v33 offset:768
	s_waitcnt vmcnt(7)
	ds_write_b32 v125, v34
	ds_write_b32 v126, v35 offset:256
	ds_write_b32 v127, v36 offset:512
	ds_write_b32 v128, v37 offset:768
	s_waitcnt vmcnt(6)
	ds_write_b32 v129, v38
	ds_write_b32 v130, v39 offset:256
	ds_write_b32 v131, v40 offset:512
	ds_write_b32 v132, v41 offset:768
	s_waitcnt vmcnt(5)
	ds_write_b32 v133, v42
	ds_write_b32 v134, v43 offset:256
	ds_write_b32 v135, v44 offset:512
	ds_write_b32 v136, v45 offset:768
	s_waitcnt vmcnt(4)
	ds_write_b32 v137, v46
	ds_write_b32 v138, v47 offset:256
	ds_write_b32 v139, v48 offset:512
	ds_write_b32 v140, v49 offset:768
	s_waitcnt vmcnt(3)
	ds_write_b32 v141, v50
	ds_write_b32 v142, v51 offset:256
	ds_write_b32 v143, v52 offset:512
	ds_write_b32 v144, v53 offset:768
	s_waitcnt vmcnt(2)
	ds_write_b32 v145, v54
	ds_write_b32 v146, v55 offset:256
	ds_write_b32 v147, v56 offset:512
	ds_write_b32 v148, v57 offset:768
	s_waitcnt vmcnt(1)
	ds_write_b32 v149, v58
	ds_write_b32 v150, v59 offset:256
	ds_write_b32 v151, v60 offset:512
	ds_write_b32 v152, v61 offset:768
	s_waitcnt vmcnt(0)
	ds_write_b32 v153, v62
	ds_write_b32 v154, v63 offset:256
	ds_write_b32 v155, v64 offset:512
	ds_write_b32 v156, v65 offset:768
	s_waitcnt lgkmcnt(0)
	s_cmp_gt_u32 s38, 2
	s_mov_b64 s[2:3], 0
	s_cbranch_scc1 .LBB0_637
	s_cmp_lg_u32 s63, 4
	s_cbranch_scc1 .LBB0_609
	s_waitcnt vmcnt(0)
	v_readfirstlane_b32 s95, v206
	s_mov_b64 s[2:3], exec
	s_mov_b64 exec, 1
	v_mov_b32_e32 v206, 4
	global_atomic_add v206, v1, v206, s[12:13] sc0
	s_mov_b64 exec, s[2:3]
	s_mov_b32 s63, 0

; DI void phase_attn(Frame& F, int l) {
;     ...
;     __syncthreads();
;     run_items1(F, 1 + l, -1, cq);
.LBB0_645:
	s_mov_b64 s[6:7], s[70:71]
	s_cmp_lg_u32 s63, 4
	s_waitcnt lgkmcnt(0)
	s_barrier
	s_cbranch_scc1 .LBB0_651
	s_waitcnt vmcnt(0)
	v_readfirstlane_b32 s95, v206
	s_mov_b64 s[2:3], exec
	s_mov_b64 exec, 1
	v_mov_b32_e32 v206, 4
	global_atomic_add v206, v1, v206, s[12:13] sc0
	s_mov_b64 exec, s[2:3]
	s_mov_b32 s63, 0

; #define LDS_WAIT() asm volatile("s_waitcnt lgkmcnt(0)" ::: "memory")
; #define RI_NEXT(D_) do { if (q.cnt == 8) { int b_ = 0; if (F.lane == 0) b_ = (int)__hip_atomic_fetch_add(qctr, 8u, __ATOMIC_RELAXED, __HIP_MEMORY_SCOPE_AGENT); q.base = __builtin_amdgcn_readfirstlane(b_); q.cnt = 0; } \
;         D_ = decode_item(KA, F.ws, kind, q.base + q.cnt); ++q.cnt; } while (0)
; DI void item_scatter(const f32x4 (&v)[16], LAS float* scr, int lane) {
;     ...
;     for (int i = 0; i < 16; ++i) { const int k = 4 * i + r4;
; #pragma unroll
;         for (int j = 0; j < 4; ++j) scr[(4 * c4 + j) * 64 + (k ^ (4 * (c4 ^ j)))] = v[i][j]; }
;     LDS_WAIT(); asm volatile("" ::: "memory");
; DI void run_items1(Frame& F, int kind, int quota, QState& q) {
;     ...
;     for (int n = 1; ; ++n) {
;         item_scatter(v, scr, F.lane);
;         TItem dn; dn.valid = false;
;         if (quota < 0 || n < quota) { RI_NEXT(dn); if (dn.valid) item_load(dn, v, F.lane); }
.LBB0_678:
	s_waitcnt vmcnt(15)
	ds_write_b32 v93, v2
	ds_write_b32 v94, v3 offset:256
	ds_write_b32 v95, v4 offset:512
	ds_write_b32 v96, v5 offset:768
	s_waitcnt vmcnt(14)
	ds_write_b32 v97, v6
	ds_write_b32 v98, v7 offset:256
	ds_write_b32 v99, v8 offset:512
	ds_write_b32 v100, v9 offset:768
	s_waitcnt vmcnt(13)
	ds_write_b32 v101, v10
	ds_write_b32 v102, v11 offset:256
	ds_write_b32 v103, v12 offset:512
	ds_write_b32 v104, v13 offset:768
	s_waitcnt vmcnt(12)
	ds_write_b32 v105, v14
	ds_write_b32 v106, v15 offset:256
	ds_write_b32 v107, v16 offset:512
	ds_write_b32 v108, v17 offset:768
	s_waitcnt vmcnt(11)
	ds_write_b32 v109, v18
	ds_write_b32 v110, v19 offset:256
	ds_write_b32 v111, v20 offset:512
	ds_write_b32 v112, v21 offset:768
	s_waitcnt vmcnt(10)
	ds_write_b32 v113, v22
	ds_write_b32 v114, v23 offset:256
	ds_write_b32 v115, v24 offset:512
	ds_write_b32 v116, v25 offset:768
	s_waitcnt vmcnt(9)
	ds_write_b32 v117, v26
	ds_write_b32 v118, v27 offset:256
	ds_write_b32 v119, v28 offset:512
	ds_write_b32 v120, v29 offset:768
	s_waitcnt vmcnt(8)
	ds_write_b32 v121, v30
	ds_write_b32 v122, v31 offset:256
	ds_write_b32 v123, v32 offset:512
	ds_write_b32 v124, v33 offset:768
	s_waitcnt vmcnt(7)
	ds_write_b32 v125, v34
	ds_write_b32 v126, v35 offset:256
	ds_write_b32 v127, v36 offset:512
	ds_write_b32 v128, v37 offset:768
	s_waitcnt vmcnt(6)
	ds_write_b32 v129, v38
	ds_write_b32 v130, v39 offset:256
	ds_write_b32 v131, v40 offset:512
	ds_write_b32 v132, v41 offset:768
	s_waitcnt vmcnt(5)
	ds_write_b32 v133, v42
	ds_write_b32 v134, v43 offset:256
	ds_write_b32 v135, v44 offset:512
	ds_write_b32 v136, v45 offset:768
	s_waitcnt vmcnt(4)
	ds_write_b32 v137, v46
	ds_write_b32 v138, v47 offset:256
	ds_write_b32 v139, v48 offset:512
	ds_write_b32 v140, v49 offset:768
	s_waitcnt vmcnt(3)
	ds_write_b32 v141, v50
	ds_write_b32 v142, v51 offset:256
	ds_write_b32 v143, v52 offset:512
	ds_write_b32 v144, v53 offset:768
	s_waitcnt vmcnt(2)
	ds_write_b32 v145, v54
	ds_write_b32 v146, v55 offset:256
	ds_write_b32 v147, v56 offset:512
	ds_write_b32 v148, v57 offset:768
	s_waitcnt vmcnt(1)
	ds_write_b32 v149, v58
	ds_write_b32 v150, v59 offset:256
	ds_write_b32 v151, v60 offset:512
	ds_write_b32 v152, v61 offset:768
	s_waitcnt vmcnt(0)
	ds_write_b32 v153, v62
	ds_write_b32 v154, v63 offset:256
	ds_write_b32 v155, v64 offset:512
	ds_write_b32 v156, v65 offset:768
	s_waitcnt lgkmcnt(0)
	s_add_i32 s63, s63, 1
	s_cmp_lg_u32 s63, 4
	s_cbranch_scc1 .LBB0_684
	s_waitcnt vmcnt(0)
	v_readfirstlane_b32 s95, v206
	s_mov_b64 s[2:3], exec
	s_mov_b64 exec, 1
	v_mov_b32_e32 v206, 4
	global_atomic_add v206, v1, v206, s[12:13] sc0
	s_mov_b64 exec, s[2:3]
	s_mov_b32 s63, 0
